# speedup vs baseline: 1.0338x; 1.0012x over previous
.Lit_A:
	ds_read_b64 v[68:69], v88
	ds_read_b64 v[70:71], v89
	ds_read_b64 v[72:73], v90
	ds_read_b64 v[74:75], v91
	v_add_u32_sdwa v92, v105, v52 dst_sel:DWORD dst_unused:UNUSED_PAD src0_sel:DWORD src1_sel:WORD_0
	v_add_u32_sdwa v93, v105, v52 dst_sel:DWORD dst_unused:UNUSED_PAD src0_sel:DWORD src1_sel:WORD_1
	v_add_u32_sdwa v106, v105, v53 dst_sel:DWORD dst_unused:UNUSED_PAD src0_sel:DWORD src1_sel:WORD_0
	v_add_u32_sdwa v107, v105, v53 dst_sel:DWORD dst_unused:UNUSED_PAD src0_sel:DWORD src1_sel:WORD_1
	v_add_u32_sdwa v108, v105, v54 dst_sel:DWORD dst_unused:UNUSED_PAD src0_sel:DWORD src1_sel:WORD_0
	v_add_u32_sdwa v109, v105, v54 dst_sel:DWORD dst_unused:UNUSED_PAD src0_sel:DWORD src1_sel:WORD_1
	v_add_u32_sdwa v88, v105, v55 dst_sel:DWORD dst_unused:UNUSED_PAD src0_sel:DWORD src1_sel:WORD_0
	v_add_u32_sdwa v89, v105, v55 dst_sel:DWORD dst_unused:UNUSED_PAD src0_sel:DWORD src1_sel:WORD_1
	ds_read_b128 v[120:123], v92
	ds_read_b128 v[124:127], v93
	ds_read_b128 v[128:131], v106
	ds_read_b128 v[132:135], v107
	ds_read_b128 v[140:143], v108
	ds_read_b128 v[144:147], v109
	ds_read_b128 v[148:151], v88
	ds_read_b128 v[152:155], v89
	s_waitcnt lgkmcnt(8)
	v_pk_add_f32 v[76:77], v[44:45], v[68:69]
	v_pk_add_f32 v[78:79], v[70:71], v[72:73]
	v_pk_add_f32 v[76:77], v[76:77], v[74:75]
	ds_read_b128 v[46:49], v138 offset:56896
	v_pk_add_f32 v[76:77], v[76:77], v[78:79]
	ds_read_b64 v[50:51], v139
	s_bitcmp1_b32 s4, 10
	s_cbranch_scc1 .Lnearslow_A

.Lfarslow_ret_A:
	v_pk_add_f32 v[120:121], v[120:121], v[128:129]
	v_pk_add_f32 v[122:123], v[122:123], v[130:131]
	v_pk_add_f32 v[140:141], v[140:141], v[148:149]
	v_pk_add_f32 v[142:143], v[142:143], v[150:151]
	v_pk_add_f32 v[120:121], v[120:121], v[140:141]
	v_pk_add_f32 v[122:123], v[122:123], v[142:143]
	v_add_u32_e32 v138, 0xfffffe00, v138
	v_add_u32_e32 v139, 0xffffff00, v139
	v_permlane32_swap_b32_e32 v120, v122
	v_permlane32_swap_b32_e32 v121, v123
	v_pk_add_f32 v[62:63], v[120:121], v[122:123]
	s_bitcmp1_b32 s4, 9
	s_cbranch_scc1 .Lslowlev_A
	s_waitcnt lgkmcnt(0)
	v_pk_fma_f32 v[80:81], v[40:41], v[82:83], v[78:79] op_sel_hi:[0,1,1]
	s_cmp_lt_u32 s9, 2
	v_pk_fma_f32 v[80:81], v[40:41], v[84:85], v[80:81] op_sel_hi:[0,1,1]
	s_mov_b64 exec, s[6:7]
	v_pk_fma_f32 v[80:81], v[40:41], v[86:87], v[80:81] op_sel_hi:[0,1,1]
	ds_write_b64 v137, v[80:81]
	s_mov_b64 exec, -1
	s_cbranch_scc1 .Lnp_A
	ds_read_b64 v[82:83], v118
	ds_read_b64 v[84:85], v119
	ds_read_b64 v[86:87], v136
	v_add_u32_sdwa v88, v116, v50 dst_sel:DWORD dst_unused:UNUSED_PAD src0_sel:DWORD src1_sel:WORD_0
	v_add_u32_sdwa v89, v116, v50 dst_sel:DWORD dst_unused:UNUSED_PAD src0_sel:DWORD src1_sel:WORD_1
	v_add_u32_sdwa v90, v116, v51 dst_sel:DWORD dst_unused:UNUSED_PAD src0_sel:DWORD src1_sel:WORD_0
	v_add_u32_sdwa v91, v116, v51 dst_sel:DWORD dst_unused:UNUSED_PAD src0_sel:DWORD src1_sel:WORD_1
	v_bfe_u32 v168, v49, 16, 7
	v_add_u32_sdwa v169, v116, v47 dst_sel:DWORD dst_unused:UNUSED_PAD src0_sel:DWORD src1_sel:WORD_0
	v_add_u32_sdwa v170, v116, v47 dst_sel:DWORD dst_unused:UNUSED_PAD src0_sel:DWORD src1_sel:WORD_1
	v_add_u32_sdwa v171, v116, v49 dst_sel:DWORD dst_unused:UNUSED_PAD src0_sel:DWORD src1_sel:WORD_0
	v_add_u32_e32 v156, 0xfffffa00, v156
	v_add_u32_e32 v172, 0xfffffe00, v137
	v_readlane_b32 s4, v60, s5
	v_max_i32_e32 v156, v156, v162
	v_lshl_add_u64 v[158:159], v[158:159], 0, s[2:3]
	s_and_b32 s23, s21, 0xff
	s_waitcnt lgkmcnt(0)
	v_pk_fma_f32 v[80:81], v[40:41], v[82:83], v[78:79] op_sel_hi:[0,1,1]
	s_cmp_lt_u32 s9, 3
	v_pk_fma_f32 v[80:81], v[40:41], v[84:85], v[80:81] op_sel_hi:[0,1,1]
	s_mov_b64 exec, s[26:27]
	v_pk_fma_f32 v[80:81], v[40:41], v[86:87], v[80:81] op_sel_hi:[0,1,1]
	ds_write_b64 v137, v[80:81]
	s_mov_b64 exec, -1
	s_cbranch_scc1 .Lbot_A
	s_mov_b32 s8, 3

.Lit_B:
	ds_read_b64 v[68:69], v88
	ds_read_b64 v[70:71], v89
	ds_read_b64 v[72:73], v90
	ds_read_b64 v[74:75], v91
	v_add_u32_sdwa v92, v105, v56 dst_sel:DWORD dst_unused:UNUSED_PAD src0_sel:DWORD src1_sel:WORD_0
	v_add_u32_sdwa v93, v105, v56 dst_sel:DWORD dst_unused:UNUSED_PAD src0_sel:DWORD src1_sel:WORD_1
	v_add_u32_sdwa v106, v105, v57 dst_sel:DWORD dst_unused:UNUSED_PAD src0_sel:DWORD src1_sel:WORD_0
	v_add_u32_sdwa v107, v105, v57 dst_sel:DWORD dst_unused:UNUSED_PAD src0_sel:DWORD src1_sel:WORD_1
	v_add_u32_sdwa v108, v105, v58 dst_sel:DWORD dst_unused:UNUSED_PAD src0_sel:DWORD src1_sel:WORD_0
	v_add_u32_sdwa v109, v105, v58 dst_sel:DWORD dst_unused:UNUSED_PAD src0_sel:DWORD src1_sel:WORD_1
	v_add_u32_sdwa v88, v105, v59 dst_sel:DWORD dst_unused:UNUSED_PAD src0_sel:DWORD src1_sel:WORD_0
	v_add_u32_sdwa v89, v105, v59 dst_sel:DWORD dst_unused:UNUSED_PAD src0_sel:DWORD src1_sel:WORD_1
	ds_read_b128 v[120:123], v92
	ds_read_b128 v[124:127], v93
	ds_read_b128 v[128:131], v106
	ds_read_b128 v[132:135], v107
	ds_read_b128 v[140:143], v108
	ds_read_b128 v[144:147], v109
	ds_read_b128 v[148:151], v88
	ds_read_b128 v[152:155], v89
	s_waitcnt lgkmcnt(8)
	v_pk_add_f32 v[76:77], v[62:63], v[68:69]
	v_pk_add_f32 v[78:79], v[70:71], v[72:73]
	v_pk_add_f32 v[76:77], v[76:77], v[74:75]
	ds_read_b128 v[38:41], v138 offset:56896
	v_pk_add_f32 v[76:77], v[76:77], v[78:79]
	ds_read_b64 v[42:43], v139
	s_bitcmp1_b32 s21, 10
	s_cbranch_scc1 .Lnearslow_B

.Lfarslow_ret_B:
	v_pk_add_f32 v[120:121], v[120:121], v[128:129]
	v_pk_add_f32 v[122:123], v[122:123], v[130:131]
	v_pk_add_f32 v[140:141], v[140:141], v[148:149]
	v_pk_add_f32 v[142:143], v[142:143], v[150:151]
	v_pk_add_f32 v[120:121], v[120:121], v[140:141]
	v_pk_add_f32 v[122:123], v[122:123], v[142:143]
	v_add_u32_e32 v138, 0xfffffe00, v138
	v_add_u32_e32 v139, 0xffffff00, v139
	v_permlane32_swap_b32_e32 v120, v122
	v_permlane32_swap_b32_e32 v121, v123
	v_pk_add_f32 v[44:45], v[120:121], v[122:123]
	s_bitcmp1_b32 s21, 9
	s_cbranch_scc1 .Lslowlev_B
	s_waitcnt lgkmcnt(0)
	v_pk_fma_f32 v[80:81], v[48:49], v[82:83], v[78:79] op_sel_hi:[0,1,1]
	s_cmp_lt_u32 s23, 2
	v_pk_fma_f32 v[80:81], v[48:49], v[84:85], v[80:81] op_sel_hi:[0,1,1]
	s_mov_b64 exec, s[6:7]
	v_pk_fma_f32 v[80:81], v[48:49], v[86:87], v[80:81] op_sel_hi:[0,1,1]
	ds_write_b64 v172, v[80:81]
	s_mov_b64 exec, -1
	s_cbranch_scc1 .Lnp_B
	ds_read_b64 v[82:83], v169
	ds_read_b64 v[84:85], v170
	ds_read_b64 v[86:87], v171
	v_add_u32_sdwa v88, v116, v42 dst_sel:DWORD dst_unused:UNUSED_PAD src0_sel:DWORD src1_sel:WORD_0
	v_add_u32_sdwa v89, v116, v42 dst_sel:DWORD dst_unused:UNUSED_PAD src0_sel:DWORD src1_sel:WORD_1
	v_add_u32_sdwa v90, v116, v43 dst_sel:DWORD dst_unused:UNUSED_PAD src0_sel:DWORD src1_sel:WORD_0
	v_add_u32_sdwa v91, v116, v43 dst_sel:DWORD dst_unused:UNUSED_PAD src0_sel:DWORD src1_sel:WORD_1
	v_bfe_u32 v117, v41, 16, 7
	v_add_u32_sdwa v118, v116, v39 dst_sel:DWORD dst_unused:UNUSED_PAD src0_sel:DWORD src1_sel:WORD_0
	v_add_u32_sdwa v119, v116, v39 dst_sel:DWORD dst_unused:UNUSED_PAD src0_sel:DWORD src1_sel:WORD_1
	v_add_u32_sdwa v136, v116, v41 dst_sel:DWORD dst_unused:UNUSED_PAD src0_sel:DWORD src1_sel:WORD_0
	v_add_u32_e32 v156, 0xfffffa00, v156
	v_add_u32_e32 v137, 0xfffffe00, v172
	v_readlane_b32 s21, v60, s5
	v_max_i32_e32 v156, v156, v162
	v_lshl_add_u64 v[158:159], v[158:159], 0, s[2:3]
	s_and_b32 s9, s4, 0xff
	s_waitcnt lgkmcnt(0)
	v_pk_fma_f32 v[80:81], v[48:49], v[82:83], v[78:79] op_sel_hi:[0,1,1]
	s_cmp_lt_u32 s23, 3
	v_pk_fma_f32 v[80:81], v[48:49], v[84:85], v[80:81] op_sel_hi:[0,1,1]
	s_mov_b64 exec, s[26:27]
	v_pk_fma_f32 v[80:81], v[48:49], v[86:87], v[80:81] op_sel_hi:[0,1,1]
	ds_write_b64 v172, v[80:81]
	s_mov_b64 exec, -1
	s_cbranch_scc1 .Lbot_B
	s_mov_b32 s8, 3
